# bundle4: + conv FIR rewritten row-major (16 independent accumulators) with interleaved LN-stat reductions
# speedup vs baseline: 1.0278x; 1.0063x over previous
.LBB0_630:
	s_or_b64 exec, exec, s[28:29]
	s_waitcnt lgkmcnt(0)
	s_barrier
	s_waitcnt vmcnt(2)
	ds_read_b64 v[10:11], v168
	ds_read_b64 v[12:13], v168 offset:2048
	ds_read_b64 v[14:15], v168 offset:4096
	ds_read_b64 v[16:17], v168 offset:6144
	ds_read_b64 v[18:19], v168 offset:8192
	ds_read_b64 v[20:21], v168 offset:10240
	ds_read_b64 v[22:23], v168 offset:12288
	ds_read_b64 v[24:25], v168 offset:14336
	ds_read_b64 v[26:27], v168 offset:16384
	s_waitcnt lgkmcnt(8)
	v_pk_fma_f32 v[60:61], v[72:73], v[10:11], v[134:135]
	ds_read_b64 v[28:29], v168 offset:18432
	s_waitcnt lgkmcnt(8)
	v_pk_fma_f32 v[60:61], v[74:75], v[12:13], v[60:61]
	v_pk_fma_f32 v[62:63], v[72:73], v[12:13], v[134:135]
	ds_read_b64 v[30:31], v168 offset:20480
	s_waitcnt lgkmcnt(8)
	v_pk_fma_f32 v[60:61], v[76:77], v[14:15], v[60:61]
	v_pk_fma_f32 v[62:63], v[74:75], v[14:15], v[62:63]
	v_pk_fma_f32 v[56:57], v[72:73], v[14:15], v[134:135]
	ds_read_b64 v[32:33], v168 offset:22528
	s_waitcnt lgkmcnt(8)
	v_pk_fma_f32 v[60:61], v[96:97], v[16:17], v[60:61]
	v_pk_fma_f32 v[62:63], v[76:77], v[16:17], v[62:63]
	v_pk_fma_f32 v[56:57], v[74:75], v[16:17], v[56:57]
	v_pk_fma_f32 v[58:59], v[72:73], v[16:17], v[134:135]
	ds_read_b64 v[10:11], v168 offset:24576
	s_waitcnt lgkmcnt(8)
	v_pk_fma_f32 v[60:61], v[78:79], v[18:19], v[60:61]
	v_pk_fma_f32 v[62:63], v[96:97], v[18:19], v[62:63]
	v_pk_fma_f32 v[56:57], v[76:77], v[18:19], v[56:57]
	v_pk_fma_f32 v[58:59], v[74:75], v[18:19], v[58:59]
	v_pk_fma_f32 v[52:53], v[72:73], v[18:19], v[134:135]
	ds_read_b64 v[12:13], v168 offset:26624
	s_waitcnt lgkmcnt(8)
	v_pk_fma_f32 v[60:61], v[80:81], v[20:21], v[60:61]
	v_pk_fma_f32 v[62:63], v[78:79], v[20:21], v[62:63]
	v_pk_fma_f32 v[56:57], v[96:97], v[20:21], v[56:57]
	v_pk_fma_f32 v[58:59], v[76:77], v[20:21], v[58:59]
	v_pk_fma_f32 v[52:53], v[74:75], v[20:21], v[52:53]
	v_pk_fma_f32 v[54:55], v[72:73], v[20:21], v[134:135]
	ds_read_b64 v[14:15], v168 offset:28672
	s_waitcnt lgkmcnt(8)
	v_pk_fma_f32 v[60:61], v[82:83], v[22:23], v[60:61]
	v_pk_fma_f32 v[62:63], v[80:81], v[22:23], v[62:63]
	v_pk_fma_f32 v[56:57], v[78:79], v[22:23], v[56:57]
	v_pk_fma_f32 v[58:59], v[96:97], v[22:23], v[58:59]
	v_pk_fma_f32 v[52:53], v[76:77], v[22:23], v[52:53]
	v_pk_fma_f32 v[54:55], v[74:75], v[22:23], v[54:55]
	v_pk_fma_f32 v[48:49], v[72:73], v[22:23], v[134:135]
	ds_read_b64 v[16:17], v168 offset:30720
	s_waitcnt lgkmcnt(8)
	v_pk_fma_f32 v[60:61], v[98:99], v[24:25], v[60:61]
	v_pk_fma_f32 v[62:63], v[82:83], v[24:25], v[62:63]
	v_pk_fma_f32 v[56:57], v[80:81], v[24:25], v[56:57]
	v_pk_fma_f32 v[58:59], v[78:79], v[24:25], v[58:59]
	v_pk_fma_f32 v[52:53], v[96:97], v[24:25], v[52:53]
	v_pk_fma_f32 v[54:55], v[76:77], v[24:25], v[54:55]
	v_pk_fma_f32 v[48:49], v[74:75], v[24:25], v[48:49]
	v_pk_fma_f32 v[50:51], v[72:73], v[24:25], v[134:135]
	ds_read_b64 v[18:19], v168 offset:32768
	s_waitcnt lgkmcnt(8)
	v_pk_fma_f32 v[60:61], v[84:85], v[26:27], v[60:61]
	v_pk_fma_f32 v[62:63], v[98:99], v[26:27], v[62:63]
	v_pk_fma_f32 v[56:57], v[82:83], v[26:27], v[56:57]
	v_pk_fma_f32 v[58:59], v[80:81], v[26:27], v[58:59]
	v_pk_fma_f32 v[52:53], v[78:79], v[26:27], v[52:53]
	v_pk_fma_f32 v[54:55], v[96:97], v[26:27], v[54:55]
	v_pk_fma_f32 v[48:49], v[76:77], v[26:27], v[48:49]
	v_pk_fma_f32 v[50:51], v[74:75], v[26:27], v[50:51]
	v_pk_fma_f32 v[166:167], v[72:73], v[26:27], v[134:135]
	ds_read_b64 v[20:21], v168 offset:34816
	s_waitcnt lgkmcnt(8)
	v_pk_fma_f32 v[60:61], v[86:87], v[28:29], v[60:61]
	v_pk_fma_f32 v[62:63], v[84:85], v[28:29], v[62:63]
	v_pk_fma_f32 v[56:57], v[98:99], v[28:29], v[56:57]
	v_pk_fma_f32 v[58:59], v[82:83], v[28:29], v[58:59]
	v_pk_fma_f32 v[52:53], v[80:81], v[28:29], v[52:53]
	v_pk_fma_f32 v[54:55], v[78:79], v[28:29], v[54:55]
	v_pk_fma_f32 v[48:49], v[96:97], v[28:29], v[48:49]
	v_pk_fma_f32 v[50:51], v[76:77], v[28:29], v[50:51]
	v_pk_fma_f32 v[166:167], v[74:75], v[28:29], v[166:167]
	v_pk_fma_f32 v[46:47], v[72:73], v[28:29], v[134:135]
	ds_read_b64 v[22:23], v168 offset:36864
	s_waitcnt lgkmcnt(8)
	v_pk_fma_f32 v[60:61], v[88:89], v[30:31], v[60:61]
	v_pk_fma_f32 v[62:63], v[86:87], v[30:31], v[62:63]
	v_pk_fma_f32 v[56:57], v[84:85], v[30:31], v[56:57]
	v_pk_fma_f32 v[58:59], v[98:99], v[30:31], v[58:59]
	v_pk_fma_f32 v[52:53], v[82:83], v[30:31], v[52:53]
	v_pk_fma_f32 v[54:55], v[80:81], v[30:31], v[54:55]
	v_pk_fma_f32 v[48:49], v[78:79], v[30:31], v[48:49]
	v_pk_fma_f32 v[50:51], v[96:97], v[30:31], v[50:51]
	v_pk_fma_f32 v[166:167], v[76:77], v[30:31], v[166:167]
	v_pk_fma_f32 v[46:47], v[74:75], v[30:31], v[46:47]
	v_pk_fma_f32 v[40:41], v[72:73], v[30:31], v[134:135]
	ds_read_b64 v[24:25], v168 offset:38912
	s_waitcnt lgkmcnt(8)
	v_pk_fma_f32 v[60:61], v[100:101], v[32:33], v[60:61]
	v_pk_fma_f32 v[62:63], v[88:89], v[32:33], v[62:63]
	v_pk_fma_f32 v[56:57], v[86:87], v[32:33], v[56:57]
	v_pk_fma_f32 v[58:59], v[84:85], v[32:33], v[58:59]
	v_pk_fma_f32 v[52:53], v[98:99], v[32:33], v[52:53]
	v_pk_fma_f32 v[54:55], v[82:83], v[32:33], v[54:55]
	v_pk_fma_f32 v[48:49], v[80:81], v[32:33], v[48:49]
	v_pk_fma_f32 v[50:51], v[78:79], v[32:33], v[50:51]
	v_pk_fma_f32 v[166:167], v[96:97], v[32:33], v[166:167]
	v_pk_fma_f32 v[46:47], v[76:77], v[32:33], v[46:47]
	v_pk_fma_f32 v[40:41], v[74:75], v[32:33], v[40:41]
	v_pk_fma_f32 v[42:43], v[72:73], v[32:33], v[134:135]
	ds_read_b64 v[26:27], v168 offset:40960
	s_waitcnt lgkmcnt(8)
	v_pk_fma_f32 v[60:61], v[90:91], v[10:11], v[60:61]
	v_pk_fma_f32 v[62:63], v[100:101], v[10:11], v[62:63]
	v_pk_fma_f32 v[56:57], v[88:89], v[10:11], v[56:57]
	v_pk_fma_f32 v[58:59], v[86:87], v[10:11], v[58:59]
	v_pk_fma_f32 v[52:53], v[84:85], v[10:11], v[52:53]
	v_pk_fma_f32 v[54:55], v[98:99], v[10:11], v[54:55]
	v_pk_fma_f32 v[48:49], v[82:83], v[10:11], v[48:49]
	v_pk_fma_f32 v[50:51], v[80:81], v[10:11], v[50:51]
	v_pk_fma_f32 v[166:167], v[78:79], v[10:11], v[166:167]
	v_pk_fma_f32 v[46:47], v[96:97], v[10:11], v[46:47]
	v_pk_fma_f32 v[40:41], v[76:77], v[10:11], v[40:41]
	v_pk_fma_f32 v[42:43], v[74:75], v[10:11], v[42:43]
	v_pk_fma_f32 v[36:37], v[72:73], v[10:11], v[134:135]
	ds_read_b64 v[28:29], v168 offset:43008
	s_waitcnt lgkmcnt(8)
	v_pk_fma_f32 v[60:61], v[92:93], v[12:13], v[60:61]
	v_pk_fma_f32 v[62:63], v[90:91], v[12:13], v[62:63]
	v_pk_fma_f32 v[56:57], v[100:101], v[12:13], v[56:57]
	v_pk_fma_f32 v[58:59], v[88:89], v[12:13], v[58:59]
	v_pk_fma_f32 v[52:53], v[86:87], v[12:13], v[52:53]
	v_pk_fma_f32 v[54:55], v[84:85], v[12:13], v[54:55]
	v_pk_fma_f32 v[48:49], v[98:99], v[12:13], v[48:49]
	v_pk_fma_f32 v[50:51], v[82:83], v[12:13], v[50:51]
	v_pk_fma_f32 v[166:167], v[80:81], v[12:13], v[166:167]
	v_pk_fma_f32 v[46:47], v[78:79], v[12:13], v[46:47]
	v_pk_fma_f32 v[40:41], v[96:97], v[12:13], v[40:41]
	v_pk_fma_f32 v[42:43], v[76:77], v[12:13], v[42:43]
	v_pk_fma_f32 v[36:37], v[74:75], v[12:13], v[36:37]
	v_pk_fma_f32 v[38:39], v[72:73], v[12:13], v[134:135]
	ds_read_b64 v[30:31], v168 offset:45056
	s_waitcnt lgkmcnt(8)
	v_pk_fma_f32 v[60:61], v[94:95], v[14:15], v[60:61]
	v_pk_fma_f32 v[62:63], v[92:93], v[14:15], v[62:63]
	v_pk_fma_f32 v[56:57], v[90:91], v[14:15], v[56:57]
	v_pk_fma_f32 v[58:59], v[100:101], v[14:15], v[58:59]
	v_pk_fma_f32 v[52:53], v[88:89], v[14:15], v[52:53]
	v_pk_fma_f32 v[54:55], v[86:87], v[14:15], v[54:55]
	v_pk_fma_f32 v[48:49], v[84:85], v[14:15], v[48:49]
	v_pk_fma_f32 v[50:51], v[98:99], v[14:15], v[50:51]
	v_pk_fma_f32 v[166:167], v[82:83], v[14:15], v[166:167]
	v_pk_fma_f32 v[46:47], v[80:81], v[14:15], v[46:47]
	v_pk_fma_f32 v[40:41], v[78:79], v[14:15], v[40:41]
	v_pk_fma_f32 v[42:43], v[96:97], v[14:15], v[42:43]
	v_pk_fma_f32 v[36:37], v[76:77], v[14:15], v[36:37]
	v_pk_fma_f32 v[38:39], v[74:75], v[14:15], v[38:39]
	v_pk_fma_f32 v[44:45], v[72:73], v[14:15], v[134:135]
	ds_read_b64 v[32:33], v168 offset:47104
	s_waitcnt lgkmcnt(8)
	v_pk_fma_f32 v[60:61], v[102:103], v[16:17], v[60:61]
	v_pk_fma_f32 v[62:63], v[94:95], v[16:17], v[62:63]
	v_pk_fma_f32 v[56:57], v[92:93], v[16:17], v[56:57]
	v_pk_fma_f32 v[58:59], v[90:91], v[16:17], v[58:59]
	v_pk_fma_f32 v[52:53], v[100:101], v[16:17], v[52:53]
	v_pk_fma_f32 v[54:55], v[88:89], v[16:17], v[54:55]
	v_pk_fma_f32 v[48:49], v[86:87], v[16:17], v[48:49]
	v_pk_fma_f32 v[50:51], v[84:85], v[16:17], v[50:51]
	v_pk_fma_f32 v[166:167], v[98:99], v[16:17], v[166:167]
	v_pk_fma_f32 v[46:47], v[82:83], v[16:17], v[46:47]
	v_pk_fma_f32 v[40:41], v[80:81], v[16:17], v[40:41]
	v_pk_fma_f32 v[42:43], v[78:79], v[16:17], v[42:43]
	v_pk_fma_f32 v[36:37], v[96:97], v[16:17], v[36:37]
	v_pk_fma_f32 v[38:39], v[76:77], v[16:17], v[38:39]
	v_pk_fma_f32 v[44:45], v[74:75], v[16:17], v[44:45]
	v_pk_fma_f32 v[8:9], v[72:73], v[16:17], v[134:135]
	ds_read_b64 v[10:11], v168 offset:49152
	s_waitcnt lgkmcnt(8)
	v_pk_fma_f32 v[60:61], v[104:105], v[18:19], v[60:61]
	v_pk_fma_f32 v[62:63], v[102:103], v[18:19], v[62:63]
	v_pk_fma_f32 v[56:57], v[94:95], v[18:19], v[56:57]
	v_pk_fma_f32 v[58:59], v[92:93], v[18:19], v[58:59]
	v_pk_fma_f32 v[52:53], v[90:91], v[18:19], v[52:53]
	v_pk_fma_f32 v[54:55], v[100:101], v[18:19], v[54:55]
	v_pk_fma_f32 v[48:49], v[88:89], v[18:19], v[48:49]
	v_pk_fma_f32 v[50:51], v[86:87], v[18:19], v[50:51]
	v_pk_fma_f32 v[166:167], v[84:85], v[18:19], v[166:167]
	v_pk_fma_f32 v[46:47], v[98:99], v[18:19], v[46:47]
	v_pk_fma_f32 v[40:41], v[82:83], v[18:19], v[40:41]
	v_pk_fma_f32 v[42:43], v[80:81], v[18:19], v[42:43]
	v_pk_fma_f32 v[36:37], v[78:79], v[18:19], v[36:37]
	v_pk_fma_f32 v[38:39], v[96:97], v[18:19], v[38:39]
	v_pk_fma_f32 v[44:45], v[76:77], v[18:19], v[44:45]
	v_pk_fma_f32 v[8:9], v[74:75], v[18:19], v[8:9]
	ds_read_b64 v[12:13], v168 offset:51200
	s_waitcnt lgkmcnt(8)
	v_pk_fma_f32 v[60:61], v[106:107], v[20:21], v[60:61]
	v_pk_fma_f32 v[62:63], v[104:105], v[20:21], v[62:63]
	v_pk_fma_f32 v[56:57], v[102:103], v[20:21], v[56:57]
	v_pk_fma_f32 v[58:59], v[94:95], v[20:21], v[58:59]
	v_pk_fma_f32 v[52:53], v[92:93], v[20:21], v[52:53]
	v_pk_fma_f32 v[54:55], v[90:91], v[20:21], v[54:55]
	v_pk_fma_f32 v[48:49], v[100:101], v[20:21], v[48:49]
	v_pk_fma_f32 v[50:51], v[88:89], v[20:21], v[50:51]
	v_pk_fma_f32 v[166:167], v[86:87], v[20:21], v[166:167]
	v_pk_fma_f32 v[46:47], v[84:85], v[20:21], v[46:47]
	v_pk_fma_f32 v[40:41], v[98:99], v[20:21], v[40:41]
	v_pk_fma_f32 v[42:43], v[82:83], v[20:21], v[42:43]
	v_pk_fma_f32 v[36:37], v[80:81], v[20:21], v[36:37]
	v_pk_fma_f32 v[38:39], v[78:79], v[20:21], v[38:39]
	v_pk_fma_f32 v[44:45], v[96:97], v[20:21], v[44:45]
	v_pk_fma_f32 v[8:9], v[76:77], v[20:21], v[8:9]
	ds_read_b64 v[14:15], v168 offset:53248
	s_waitcnt lgkmcnt(8)
	v_pk_fma_f32 v[60:61], v[108:109], v[22:23], v[60:61]
	v_pk_fma_f32 v[62:63], v[106:107], v[22:23], v[62:63]
	v_pk_fma_f32 v[56:57], v[104:105], v[22:23], v[56:57]
	v_pk_fma_f32 v[58:59], v[102:103], v[22:23], v[58:59]
	v_pk_fma_f32 v[52:53], v[94:95], v[22:23], v[52:53]
	v_pk_fma_f32 v[54:55], v[92:93], v[22:23], v[54:55]
	v_pk_fma_f32 v[48:49], v[90:91], v[22:23], v[48:49]
	v_pk_fma_f32 v[50:51], v[100:101], v[22:23], v[50:51]
	v_pk_fma_f32 v[166:167], v[88:89], v[22:23], v[166:167]
	v_pk_fma_f32 v[46:47], v[86:87], v[22:23], v[46:47]
	v_pk_fma_f32 v[40:41], v[84:85], v[22:23], v[40:41]
	v_pk_fma_f32 v[42:43], v[98:99], v[22:23], v[42:43]
	v_pk_fma_f32 v[36:37], v[82:83], v[22:23], v[36:37]
	v_pk_fma_f32 v[38:39], v[80:81], v[22:23], v[38:39]
	v_pk_fma_f32 v[44:45], v[78:79], v[22:23], v[44:45]
	v_pk_fma_f32 v[8:9], v[96:97], v[22:23], v[8:9]
	ds_read_b64 v[16:17], v168 offset:55296
	s_waitcnt lgkmcnt(8)
	v_pk_fma_f32 v[60:61], v[126:127], v[24:25], v[60:61]
	v_pk_fma_f32 v[62:63], v[108:109], v[24:25], v[62:63]
	v_pk_fma_f32 v[56:57], v[106:107], v[24:25], v[56:57]
	v_pk_fma_f32 v[58:59], v[104:105], v[24:25], v[58:59]
	v_pk_fma_f32 v[52:53], v[102:103], v[24:25], v[52:53]
	v_pk_fma_f32 v[54:55], v[94:95], v[24:25], v[54:55]
	v_pk_fma_f32 v[48:49], v[92:93], v[24:25], v[48:49]
	v_pk_fma_f32 v[50:51], v[90:91], v[24:25], v[50:51]
	v_pk_fma_f32 v[166:167], v[100:101], v[24:25], v[166:167]
	v_pk_fma_f32 v[46:47], v[88:89], v[24:25], v[46:47]
	v_pk_fma_f32 v[40:41], v[86:87], v[24:25], v[40:41]
	v_pk_fma_f32 v[42:43], v[84:85], v[24:25], v[42:43]
	v_pk_fma_f32 v[36:37], v[98:99], v[24:25], v[36:37]
	v_pk_fma_f32 v[38:39], v[82:83], v[24:25], v[38:39]
	v_pk_fma_f32 v[44:45], v[80:81], v[24:25], v[44:45]
	v_pk_fma_f32 v[8:9], v[78:79], v[24:25], v[8:9]
	ds_read_b64 v[18:19], v168 offset:57344
	s_waitcnt lgkmcnt(8)
	v_pk_fma_f32 v[60:61], v[110:111], v[26:27], v[60:61]
	v_pk_fma_f32 v[62:63], v[126:127], v[26:27], v[62:63]
	v_pk_fma_f32 v[56:57], v[108:109], v[26:27], v[56:57]
	v_pk_fma_f32 v[58:59], v[106:107], v[26:27], v[58:59]
	v_pk_fma_f32 v[52:53], v[104:105], v[26:27], v[52:53]
	v_pk_fma_f32 v[54:55], v[102:103], v[26:27], v[54:55]
	v_pk_fma_f32 v[48:49], v[94:95], v[26:27], v[48:49]
	v_pk_fma_f32 v[50:51], v[92:93], v[26:27], v[50:51]
	v_pk_fma_f32 v[166:167], v[90:91], v[26:27], v[166:167]
	v_pk_fma_f32 v[46:47], v[100:101], v[26:27], v[46:47]
	v_pk_fma_f32 v[40:41], v[88:89], v[26:27], v[40:41]
	v_pk_fma_f32 v[42:43], v[86:87], v[26:27], v[42:43]
	v_pk_fma_f32 v[36:37], v[84:85], v[26:27], v[36:37]
	v_pk_fma_f32 v[38:39], v[98:99], v[26:27], v[38:39]
	v_pk_fma_f32 v[44:45], v[82:83], v[26:27], v[44:45]
	v_pk_fma_f32 v[8:9], v[80:81], v[26:27], v[8:9]
	ds_read_b64 v[20:21], v168 offset:59392
	s_waitcnt lgkmcnt(8)
	v_pk_fma_f32 v[60:61], v[112:113], v[28:29], v[60:61]
	v_pk_fma_f32 v[62:63], v[110:111], v[28:29], v[62:63]
	v_pk_fma_f32 v[56:57], v[126:127], v[28:29], v[56:57]
	v_pk_fma_f32 v[58:59], v[108:109], v[28:29], v[58:59]
	v_pk_fma_f32 v[52:53], v[106:107], v[28:29], v[52:53]
	v_pk_fma_f32 v[54:55], v[104:105], v[28:29], v[54:55]
	v_pk_fma_f32 v[48:49], v[102:103], v[28:29], v[48:49]
	v_pk_fma_f32 v[50:51], v[94:95], v[28:29], v[50:51]
	v_pk_fma_f32 v[166:167], v[92:93], v[28:29], v[166:167]
	v_pk_fma_f32 v[46:47], v[90:91], v[28:29], v[46:47]
	v_pk_fma_f32 v[40:41], v[100:101], v[28:29], v[40:41]
	v_pk_fma_f32 v[42:43], v[88:89], v[28:29], v[42:43]
	v_pk_fma_f32 v[36:37], v[86:87], v[28:29], v[36:37]
	v_pk_fma_f32 v[38:39], v[84:85], v[28:29], v[38:39]
	v_pk_fma_f32 v[44:45], v[98:99], v[28:29], v[44:45]
	v_pk_fma_f32 v[8:9], v[82:83], v[28:29], v[8:9]
	ds_read_b64 v[22:23], v168 offset:61440
	s_waitcnt lgkmcnt(8)
	v_pk_fma_f32 v[60:61], v[114:115], v[30:31], v[60:61]
	v_pk_fma_f32 v[62:63], v[112:113], v[30:31], v[62:63]
	v_pk_fma_f32 v[56:57], v[110:111], v[30:31], v[56:57]
	v_pk_fma_f32 v[58:59], v[126:127], v[30:31], v[58:59]
	v_pk_fma_f32 v[52:53], v[108:109], v[30:31], v[52:53]
	v_pk_fma_f32 v[54:55], v[106:107], v[30:31], v[54:55]
	v_pk_fma_f32 v[48:49], v[104:105], v[30:31], v[48:49]
	v_pk_fma_f32 v[50:51], v[102:103], v[30:31], v[50:51]
	v_pk_fma_f32 v[166:167], v[94:95], v[30:31], v[166:167]
	v_pk_fma_f32 v[46:47], v[92:93], v[30:31], v[46:47]
	v_pk_fma_f32 v[40:41], v[90:91], v[30:31], v[40:41]
	v_pk_fma_f32 v[42:43], v[100:101], v[30:31], v[42:43]
	v_pk_fma_f32 v[36:37], v[88:89], v[30:31], v[36:37]
	v_pk_fma_f32 v[38:39], v[86:87], v[30:31], v[38:39]
	v_pk_fma_f32 v[44:45], v[84:85], v[30:31], v[44:45]
	v_pk_fma_f32 v[8:9], v[98:99], v[30:31], v[8:9]
	ds_read_b64 v[24:25], v168 offset:63488
	s_waitcnt lgkmcnt(8)
	v_pk_fma_f32 v[60:61], v[128:129], v[32:33], v[60:61]
	v_pk_fma_f32 v[62:63], v[114:115], v[32:33], v[62:63]
	v_pk_fma_f32 v[56:57], v[112:113], v[32:33], v[56:57]
	v_pk_fma_f32 v[58:59], v[110:111], v[32:33], v[58:59]
	v_pk_fma_f32 v[52:53], v[126:127], v[32:33], v[52:53]
	v_pk_fma_f32 v[54:55], v[108:109], v[32:33], v[54:55]
	v_pk_fma_f32 v[48:49], v[106:107], v[32:33], v[48:49]
	v_pk_fma_f32 v[50:51], v[104:105], v[32:33], v[50:51]
	v_pk_fma_f32 v[166:167], v[102:103], v[32:33], v[166:167]
	v_pk_fma_f32 v[46:47], v[94:95], v[32:33], v[46:47]
	v_pk_fma_f32 v[40:41], v[92:93], v[32:33], v[40:41]
	v_pk_fma_f32 v[42:43], v[90:91], v[32:33], v[42:43]
	v_pk_fma_f32 v[36:37], v[100:101], v[32:33], v[36:37]
	v_pk_fma_f32 v[38:39], v[88:89], v[32:33], v[38:39]
	v_pk_fma_f32 v[44:45], v[86:87], v[32:33], v[44:45]
	v_pk_fma_f32 v[8:9], v[84:85], v[32:33], v[8:9]
	ds_read_b64 v[26:27], v170
	s_waitcnt lgkmcnt(8)
	v_pk_fma_f32 v[60:61], v[116:117], v[10:11], v[60:61]
	v_pk_fma_f32 v[62:63], v[128:129], v[10:11], v[62:63]
	v_pk_fma_f32 v[56:57], v[114:115], v[10:11], v[56:57]
	v_pk_fma_f32 v[58:59], v[112:113], v[10:11], v[58:59]
	v_pk_fma_f32 v[52:53], v[110:111], v[10:11], v[52:53]
	v_pk_fma_f32 v[54:55], v[126:127], v[10:11], v[54:55]
	v_pk_fma_f32 v[48:49], v[108:109], v[10:11], v[48:49]
	v_pk_fma_f32 v[50:51], v[106:107], v[10:11], v[50:51]
	v_pk_fma_f32 v[166:167], v[104:105], v[10:11], v[166:167]
	v_pk_fma_f32 v[46:47], v[102:103], v[10:11], v[46:47]
	v_pk_fma_f32 v[40:41], v[94:95], v[10:11], v[40:41]
	v_pk_fma_f32 v[42:43], v[92:93], v[10:11], v[42:43]
	v_pk_fma_f32 v[36:37], v[90:91], v[10:11], v[36:37]
	v_pk_fma_f32 v[38:39], v[100:101], v[10:11], v[38:39]
	v_pk_fma_f32 v[44:45], v[88:89], v[10:11], v[44:45]
	v_pk_fma_f32 v[8:9], v[86:87], v[10:11], v[8:9]
	ds_read_b64 v[28:29], v171
	s_waitcnt lgkmcnt(8)
	v_pk_fma_f32 v[60:61], v[118:119], v[12:13], v[60:61]
	v_pk_fma_f32 v[62:63], v[116:117], v[12:13], v[62:63]
	v_pk_fma_f32 v[56:57], v[128:129], v[12:13], v[56:57]
	v_pk_fma_f32 v[58:59], v[114:115], v[12:13], v[58:59]
	v_pk_fma_f32 v[52:53], v[112:113], v[12:13], v[52:53]
	v_pk_fma_f32 v[54:55], v[110:111], v[12:13], v[54:55]
	v_pk_fma_f32 v[48:49], v[126:127], v[12:13], v[48:49]
	v_pk_fma_f32 v[50:51], v[108:109], v[12:13], v[50:51]
	v_pk_fma_f32 v[166:167], v[106:107], v[12:13], v[166:167]
	v_pk_fma_f32 v[46:47], v[104:105], v[12:13], v[46:47]
	v_pk_fma_f32 v[40:41], v[102:103], v[12:13], v[40:41]
	v_pk_fma_f32 v[42:43], v[94:95], v[12:13], v[42:43]
	v_pk_fma_f32 v[36:37], v[92:93], v[12:13], v[36:37]
	v_pk_fma_f32 v[38:39], v[90:91], v[12:13], v[38:39]
	v_pk_fma_f32 v[44:45], v[100:101], v[12:13], v[44:45]
	v_pk_fma_f32 v[8:9], v[88:89], v[12:13], v[8:9]
	ds_read_b64 v[30:31], v172
	s_waitcnt lgkmcnt(8)
	v_pk_fma_f32 v[60:61], v[120:121], v[14:15], v[60:61]
	v_pk_fma_f32 v[62:63], v[118:119], v[14:15], v[62:63]
	v_pk_fma_f32 v[56:57], v[116:117], v[14:15], v[56:57]
	v_pk_fma_f32 v[58:59], v[128:129], v[14:15], v[58:59]
	v_pk_fma_f32 v[52:53], v[114:115], v[14:15], v[52:53]
	v_pk_fma_f32 v[54:55], v[112:113], v[14:15], v[54:55]
	v_pk_fma_f32 v[48:49], v[110:111], v[14:15], v[48:49]
	v_pk_fma_f32 v[50:51], v[126:127], v[14:15], v[50:51]
	v_pk_fma_f32 v[166:167], v[108:109], v[14:15], v[166:167]
	v_pk_fma_f32 v[46:47], v[106:107], v[14:15], v[46:47]
	v_pk_fma_f32 v[40:41], v[104:105], v[14:15], v[40:41]
	v_pk_fma_f32 v[42:43], v[102:103], v[14:15], v[42:43]
	v_pk_fma_f32 v[36:37], v[94:95], v[14:15], v[36:37]
	v_pk_fma_f32 v[38:39], v[92:93], v[14:15], v[38:39]
	v_pk_fma_f32 v[44:45], v[90:91], v[14:15], v[44:45]
	v_pk_fma_f32 v[8:9], v[100:101], v[14:15], v[8:9]
	ds_read_b64 v[32:33], v173
	s_waitcnt lgkmcnt(8)
	v_pk_fma_f32 v[60:61], v[130:131], v[16:17], v[60:61]
	v_pk_fma_f32 v[62:63], v[120:121], v[16:17], v[62:63]
	v_pk_fma_f32 v[56:57], v[118:119], v[16:17], v[56:57]
	v_pk_fma_f32 v[58:59], v[116:117], v[16:17], v[58:59]
	v_pk_fma_f32 v[52:53], v[128:129], v[16:17], v[52:53]
	v_pk_fma_f32 v[54:55], v[114:115], v[16:17], v[54:55]
	v_pk_fma_f32 v[48:49], v[112:113], v[16:17], v[48:49]
	v_pk_fma_f32 v[50:51], v[110:111], v[16:17], v[50:51]
	v_pk_fma_f32 v[166:167], v[126:127], v[16:17], v[166:167]
	v_pk_fma_f32 v[46:47], v[108:109], v[16:17], v[46:47]
	v_pk_fma_f32 v[40:41], v[106:107], v[16:17], v[40:41]
	v_pk_fma_f32 v[42:43], v[104:105], v[16:17], v[42:43]
	v_pk_fma_f32 v[36:37], v[102:103], v[16:17], v[36:37]
	v_pk_fma_f32 v[38:39], v[94:95], v[16:17], v[38:39]
	v_pk_fma_f32 v[44:45], v[92:93], v[16:17], v[44:45]
	v_pk_fma_f32 v[8:9], v[90:91], v[16:17], v[8:9]
	ds_read_b64 v[10:11], v174
	s_waitcnt lgkmcnt(8)
	v_pk_fma_f32 v[60:61], v[122:123], v[18:19], v[60:61]
	v_pk_fma_f32 v[62:63], v[130:131], v[18:19], v[62:63]
	v_pk_fma_f32 v[56:57], v[120:121], v[18:19], v[56:57]
	v_pk_fma_f32 v[58:59], v[118:119], v[18:19], v[58:59]
	v_pk_fma_f32 v[52:53], v[116:117], v[18:19], v[52:53]
	v_pk_fma_f32 v[54:55], v[128:129], v[18:19], v[54:55]
	v_pk_fma_f32 v[48:49], v[114:115], v[18:19], v[48:49]
	v_pk_fma_f32 v[50:51], v[112:113], v[18:19], v[50:51]
	v_pk_fma_f32 v[166:167], v[110:111], v[18:19], v[166:167]
	v_pk_fma_f32 v[46:47], v[126:127], v[18:19], v[46:47]
	v_pk_fma_f32 v[40:41], v[108:109], v[18:19], v[40:41]
	v_pk_fma_f32 v[42:43], v[106:107], v[18:19], v[42:43]
	v_pk_fma_f32 v[36:37], v[104:105], v[18:19], v[36:37]
	v_pk_fma_f32 v[38:39], v[102:103], v[18:19], v[38:39]
	v_pk_fma_f32 v[44:45], v[94:95], v[18:19], v[44:45]
	v_pk_fma_f32 v[8:9], v[92:93], v[18:19], v[8:9]
	ds_read_b64 v[12:13], v175
	s_waitcnt lgkmcnt(8)
	v_pk_fma_f32 v[60:61], v[124:125], v[20:21], v[60:61]
	v_pk_fma_f32 v[62:63], v[122:123], v[20:21], v[62:63]
	v_pk_fma_f32 v[56:57], v[130:131], v[20:21], v[56:57]
	v_pk_fma_f32 v[58:59], v[120:121], v[20:21], v[58:59]
	v_pk_fma_f32 v[52:53], v[118:119], v[20:21], v[52:53]
	v_pk_fma_f32 v[54:55], v[116:117], v[20:21], v[54:55]
	v_pk_fma_f32 v[48:49], v[128:129], v[20:21], v[48:49]
	v_pk_fma_f32 v[50:51], v[114:115], v[20:21], v[50:51]
	v_pk_fma_f32 v[166:167], v[112:113], v[20:21], v[166:167]
	v_pk_fma_f32 v[46:47], v[110:111], v[20:21], v[46:47]
	v_pk_fma_f32 v[40:41], v[126:127], v[20:21], v[40:41]
	v_pk_fma_f32 v[42:43], v[108:109], v[20:21], v[42:43]
	v_pk_fma_f32 v[36:37], v[106:107], v[20:21], v[36:37]
	v_pk_fma_f32 v[38:39], v[104:105], v[20:21], v[38:39]
	v_pk_fma_f32 v[44:45], v[102:103], v[20:21], v[44:45]
	v_pk_fma_f32 v[8:9], v[94:95], v[20:21], v[8:9]
	ds_read_b64 v[14:15], v176
	s_waitcnt lgkmcnt(8)
	v_pk_fma_f32 v[60:61], v[132:133], v[22:23], v[60:61]
	v_pk_fma_f32 v[62:63], v[124:125], v[22:23], v[62:63]
	v_pk_fma_f32 v[56:57], v[122:123], v[22:23], v[56:57]
	v_pk_fma_f32 v[58:59], v[130:131], v[22:23], v[58:59]
	v_pk_fma_f32 v[52:53], v[120:121], v[22:23], v[52:53]
	v_pk_fma_f32 v[54:55], v[118:119], v[22:23], v[54:55]
	v_pk_fma_f32 v[48:49], v[116:117], v[22:23], v[48:49]
	v_pk_fma_f32 v[50:51], v[128:129], v[22:23], v[50:51]
	v_pk_fma_f32 v[166:167], v[114:115], v[22:23], v[166:167]
	v_pk_fma_f32 v[46:47], v[112:113], v[22:23], v[46:47]
	v_pk_fma_f32 v[40:41], v[110:111], v[22:23], v[40:41]
	v_pk_fma_f32 v[42:43], v[126:127], v[22:23], v[42:43]
	v_pk_fma_f32 v[36:37], v[108:109], v[22:23], v[36:37]
	v_pk_fma_f32 v[38:39], v[106:107], v[22:23], v[38:39]
	v_pk_fma_f32 v[44:45], v[104:105], v[22:23], v[44:45]
	v_pk_fma_f32 v[8:9], v[102:103], v[22:23], v[8:9]
	ds_read_b64 v[16:17], v177
	s_waitcnt lgkmcnt(8)
	v_pk_fma_f32 v[62:63], v[132:133], v[24:25], v[62:63]
	v_pk_fma_f32 v[56:57], v[124:125], v[24:25], v[56:57]
	v_pk_fma_f32 v[58:59], v[122:123], v[24:25], v[58:59]
	v_pk_fma_f32 v[52:53], v[130:131], v[24:25], v[52:53]
	v_pk_fma_f32 v[54:55], v[120:121], v[24:25], v[54:55]
	v_pk_fma_f32 v[48:49], v[118:119], v[24:25], v[48:49]
	v_pk_fma_f32 v[50:51], v[116:117], v[24:25], v[50:51]
	v_pk_fma_f32 v[166:167], v[128:129], v[24:25], v[166:167]
	v_pk_fma_f32 v[46:47], v[114:115], v[24:25], v[46:47]
	v_pk_fma_f32 v[40:41], v[112:113], v[24:25], v[40:41]
	v_pk_fma_f32 v[42:43], v[110:111], v[24:25], v[42:43]
	v_pk_fma_f32 v[36:37], v[126:127], v[24:25], v[36:37]
	v_pk_fma_f32 v[38:39], v[108:109], v[24:25], v[38:39]
	v_pk_fma_f32 v[44:45], v[106:107], v[24:25], v[44:45]
	v_pk_fma_f32 v[8:9], v[104:105], v[24:25], v[8:9]
	ds_read_b64 v[18:19], v178
	s_waitcnt lgkmcnt(8)
	v_pk_fma_f32 v[56:57], v[132:133], v[26:27], v[56:57]
	v_pk_fma_f32 v[58:59], v[124:125], v[26:27], v[58:59]
	v_pk_fma_f32 v[52:53], v[122:123], v[26:27], v[52:53]
	v_pk_fma_f32 v[54:55], v[130:131], v[26:27], v[54:55]
	v_pk_fma_f32 v[48:49], v[120:121], v[26:27], v[48:49]
	v_pk_fma_f32 v[50:51], v[118:119], v[26:27], v[50:51]
	v_pk_fma_f32 v[166:167], v[116:117], v[26:27], v[166:167]
	v_pk_fma_f32 v[46:47], v[128:129], v[26:27], v[46:47]
	v_pk_fma_f32 v[40:41], v[114:115], v[26:27], v[40:41]
	v_pk_fma_f32 v[42:43], v[112:113], v[26:27], v[42:43]
	v_pk_fma_f32 v[36:37], v[110:111], v[26:27], v[36:37]
	v_pk_fma_f32 v[38:39], v[126:127], v[26:27], v[38:39]
	v_pk_fma_f32 v[44:45], v[108:109], v[26:27], v[44:45]
	v_pk_fma_f32 v[8:9], v[106:107], v[26:27], v[8:9]
	ds_read_b64 v[20:21], v179
	s_waitcnt lgkmcnt(8)
	v_pk_fma_f32 v[58:59], v[132:133], v[28:29], v[58:59]
	v_pk_fma_f32 v[52:53], v[124:125], v[28:29], v[52:53]
	v_pk_fma_f32 v[54:55], v[122:123], v[28:29], v[54:55]
	v_pk_fma_f32 v[48:49], v[130:131], v[28:29], v[48:49]
	v_pk_fma_f32 v[50:51], v[120:121], v[28:29], v[50:51]
	v_pk_fma_f32 v[166:167], v[118:119], v[28:29], v[166:167]
	v_pk_fma_f32 v[46:47], v[116:117], v[28:29], v[46:47]
	v_pk_fma_f32 v[40:41], v[128:129], v[28:29], v[40:41]
	v_pk_fma_f32 v[42:43], v[114:115], v[28:29], v[42:43]
	v_pk_fma_f32 v[36:37], v[112:113], v[28:29], v[36:37]
	v_pk_fma_f32 v[38:39], v[110:111], v[28:29], v[38:39]
	v_pk_fma_f32 v[44:45], v[126:127], v[28:29], v[44:45]
	v_pk_fma_f32 v[8:9], v[108:109], v[28:29], v[8:9]
	ds_read_b64 v[22:23], v180
	s_waitcnt lgkmcnt(8)
	v_pk_fma_f32 v[52:53], v[132:133], v[30:31], v[52:53]
	v_pk_fma_f32 v[54:55], v[124:125], v[30:31], v[54:55]
	v_pk_fma_f32 v[48:49], v[122:123], v[30:31], v[48:49]
	v_pk_fma_f32 v[50:51], v[130:131], v[30:31], v[50:51]
	v_pk_fma_f32 v[166:167], v[120:121], v[30:31], v[166:167]
	v_pk_fma_f32 v[46:47], v[118:119], v[30:31], v[46:47]
	v_pk_fma_f32 v[40:41], v[116:117], v[30:31], v[40:41]
	v_pk_fma_f32 v[42:43], v[128:129], v[30:31], v[42:43]
	v_pk_fma_f32 v[36:37], v[114:115], v[30:31], v[36:37]
	v_pk_fma_f32 v[38:39], v[112:113], v[30:31], v[38:39]
	v_pk_fma_f32 v[44:45], v[110:111], v[30:31], v[44:45]
	v_pk_fma_f32 v[8:9], v[126:127], v[30:31], v[8:9]
	ds_read_b64 v[24:25], v181
	s_waitcnt lgkmcnt(8)
	v_pk_fma_f32 v[54:55], v[132:133], v[32:33], v[54:55]
	v_pk_fma_f32 v[48:49], v[124:125], v[32:33], v[48:49]
	v_pk_fma_f32 v[50:51], v[122:123], v[32:33], v[50:51]
	v_pk_fma_f32 v[166:167], v[130:131], v[32:33], v[166:167]
	v_pk_fma_f32 v[46:47], v[120:121], v[32:33], v[46:47]
	v_pk_fma_f32 v[40:41], v[118:119], v[32:33], v[40:41]
	v_pk_fma_f32 v[42:43], v[116:117], v[32:33], v[42:43]
	v_pk_fma_f32 v[36:37], v[128:129], v[32:33], v[36:37]
	v_pk_fma_f32 v[38:39], v[114:115], v[32:33], v[38:39]
	v_pk_fma_f32 v[44:45], v[112:113], v[32:33], v[44:45]
	v_pk_fma_f32 v[8:9], v[110:111], v[32:33], v[8:9]
	ds_read_b64 v[26:27], v182
	s_waitcnt lgkmcnt(8)
	v_pk_fma_f32 v[48:49], v[132:133], v[10:11], v[48:49]
	v_pk_fma_f32 v[50:51], v[124:125], v[10:11], v[50:51]
	v_pk_fma_f32 v[166:167], v[122:123], v[10:11], v[166:167]
	v_pk_fma_f32 v[46:47], v[130:131], v[10:11], v[46:47]
	v_pk_fma_f32 v[40:41], v[120:121], v[10:11], v[40:41]
	v_pk_fma_f32 v[42:43], v[118:119], v[10:11], v[42:43]
	v_pk_fma_f32 v[36:37], v[116:117], v[10:11], v[36:37]
	v_pk_fma_f32 v[38:39], v[128:129], v[10:11], v[38:39]
	v_pk_fma_f32 v[44:45], v[114:115], v[10:11], v[44:45]
	v_pk_fma_f32 v[8:9], v[112:113], v[10:11], v[8:9]
	ds_read_b64 v[28:29], v183
	s_waitcnt lgkmcnt(8)
	v_pk_fma_f32 v[50:51], v[132:133], v[12:13], v[50:51]
	v_pk_fma_f32 v[166:167], v[124:125], v[12:13], v[166:167]
	v_pk_fma_f32 v[46:47], v[122:123], v[12:13], v[46:47]
	v_pk_fma_f32 v[40:41], v[130:131], v[12:13], v[40:41]
	v_pk_fma_f32 v[42:43], v[120:121], v[12:13], v[42:43]
	v_pk_fma_f32 v[36:37], v[118:119], v[12:13], v[36:37]
	v_pk_fma_f32 v[38:39], v[116:117], v[12:13], v[38:39]
	v_pk_fma_f32 v[44:45], v[128:129], v[12:13], v[44:45]
	v_pk_fma_f32 v[8:9], v[114:115], v[12:13], v[8:9]
	s_waitcnt lgkmcnt(7)
	v_pk_fma_f32 v[166:167], v[132:133], v[14:15], v[166:167]
	v_pk_fma_f32 v[46:47], v[124:125], v[14:15], v[46:47]
	v_pk_fma_f32 v[40:41], v[122:123], v[14:15], v[40:41]
	v_pk_fma_f32 v[42:43], v[130:131], v[14:15], v[42:43]
	v_pk_fma_f32 v[36:37], v[120:121], v[14:15], v[36:37]
	v_pk_fma_f32 v[38:39], v[118:119], v[14:15], v[38:39]
	v_pk_fma_f32 v[44:45], v[116:117], v[14:15], v[44:45]
	v_pk_fma_f32 v[8:9], v[128:129], v[14:15], v[8:9]
	s_waitcnt lgkmcnt(6)
	v_pk_fma_f32 v[46:47], v[132:133], v[16:17], v[46:47]
	v_pk_fma_f32 v[40:41], v[124:125], v[16:17], v[40:41]
	v_pk_fma_f32 v[42:43], v[122:123], v[16:17], v[42:43]
	v_pk_fma_f32 v[36:37], v[130:131], v[16:17], v[36:37]
	v_pk_fma_f32 v[38:39], v[120:121], v[16:17], v[38:39]
	v_pk_fma_f32 v[44:45], v[118:119], v[16:17], v[44:45]
	v_pk_fma_f32 v[8:9], v[116:117], v[16:17], v[8:9]
	s_waitcnt lgkmcnt(5)
	v_pk_fma_f32 v[40:41], v[132:133], v[18:19], v[40:41]
	v_pk_fma_f32 v[42:43], v[124:125], v[18:19], v[42:43]
	v_pk_fma_f32 v[36:37], v[122:123], v[18:19], v[36:37]
	v_pk_fma_f32 v[38:39], v[130:131], v[18:19], v[38:39]
	v_pk_fma_f32 v[44:45], v[120:121], v[18:19], v[44:45]
	v_pk_fma_f32 v[8:9], v[118:119], v[18:19], v[8:9]
	s_waitcnt lgkmcnt(4)
	v_pk_fma_f32 v[42:43], v[132:133], v[20:21], v[42:43]
	v_pk_fma_f32 v[36:37], v[124:125], v[20:21], v[36:37]
	v_pk_fma_f32 v[38:39], v[122:123], v[20:21], v[38:39]
	v_pk_fma_f32 v[44:45], v[130:131], v[20:21], v[44:45]
	v_pk_fma_f32 v[8:9], v[120:121], v[20:21], v[8:9]
	s_waitcnt lgkmcnt(3)
	v_pk_fma_f32 v[36:37], v[132:133], v[22:23], v[36:37]
	v_pk_fma_f32 v[38:39], v[124:125], v[22:23], v[38:39]
	v_pk_fma_f32 v[44:45], v[122:123], v[22:23], v[44:45]
	v_pk_fma_f32 v[8:9], v[130:131], v[22:23], v[8:9]
	s_waitcnt lgkmcnt(2)
	v_pk_fma_f32 v[38:39], v[132:133], v[24:25], v[38:39]
	v_pk_fma_f32 v[44:45], v[124:125], v[24:25], v[44:45]
	v_pk_fma_f32 v[8:9], v[122:123], v[24:25], v[8:9]
	s_waitcnt lgkmcnt(1)
	v_pk_fma_f32 v[44:45], v[132:133], v[26:27], v[44:45]
	v_pk_fma_f32 v[8:9], v[124:125], v[26:27], v[8:9]
	s_waitcnt lgkmcnt(0)
	v_pk_fma_f32 v[8:9], v[132:133], v[28:29], v[8:9]
	v_pk_mul_f32 v[10:11], v[60:61], v[60:61]
	v_pk_mul_f32 v[12:13], v[62:63], v[62:63]
	v_pk_mul_f32 v[14:15], v[56:57], v[56:57]
	v_pk_mul_f32 v[16:17], v[58:59], v[58:59]
	v_pk_mul_f32 v[18:19], v[52:53], v[52:53]
	v_pk_mul_f32 v[20:21], v[54:55], v[54:55]
	v_pk_mul_f32 v[22:23], v[48:49], v[48:49]
	v_pk_mul_f32 v[24:25], v[50:51], v[50:51]
	v_pk_mul_f32 v[26:27], v[166:167], v[166:167]
	v_pk_mul_f32 v[28:29], v[46:47], v[46:47]
	v_pk_mul_f32 v[30:31], v[40:41], v[40:41]
	v_pk_mul_f32 v[32:33], v[42:43], v[42:43]
	v_pk_mul_f32 v[0:1], v[36:37], v[36:37]
	v_pk_mul_f32 v[2:3], v[38:39], v[38:39]
	v_pk_mul_f32 v[4:5], v[44:45], v[44:45]
	v_pk_mul_f32 v[6:7], v[8:9], v[8:9]
	v_add_f32_e32 v11, v10, v11
	v_add_f32_e32 v13, v12, v13
	v_add_f32_e32 v15, v14, v15
	v_add_f32_e32 v17, v16, v17
	v_add_f32_e32 v19, v18, v19
	v_add_f32_e32 v21, v20, v21
	v_add_f32_e32 v23, v22, v23
	v_add_f32_e32 v25, v24, v25
	v_add_f32_e32 v27, v26, v27
	v_add_f32_e32 v29, v28, v29
	v_add_f32_e32 v31, v30, v31
	v_add_f32_e32 v33, v32, v33
	v_add_f32_e32 v1, v0, v1
	v_add_f32_e32 v3, v2, v3
	v_add_f32_e32 v5, v4, v5
	v_add_f32_e32 v7, v6, v7
	v_add_f32_e32 v10, v60, v61
	v_add_f32_e32 v12, v62, v63
	v_add_f32_e32 v14, v56, v57
	v_add_f32_e32 v16, v58, v59
	v_add_f32_e32 v18, v52, v53
	v_add_f32_e32 v20, v54, v55
	v_add_f32_e32 v22, v48, v49
	v_add_f32_e32 v24, v50, v51
	v_add_f32_e32 v26, v166, v167
	v_add_f32_e32 v28, v46, v47
	v_add_f32_e32 v30, v40, v41
	v_add_f32_e32 v32, v42, v43
	v_add_f32_e32 v0, v36, v37
	v_add_f32_e32 v2, v38, v39
	v_add_f32_e32 v4, v44, v45
	v_add_f32_e32 v6, v8, v9
	v_add_f32_dpp v10, v10, v10 quad_perm:[1,0,3,2] row_mask:0xf bank_mask:0xf bound_ctrl:1
	v_add_f32_dpp v11, v11, v11 quad_perm:[1,0,3,2] row_mask:0xf bank_mask:0xf bound_ctrl:1
	v_add_f32_dpp v12, v12, v12 quad_perm:[1,0,3,2] row_mask:0xf bank_mask:0xf bound_ctrl:1
	v_add_f32_dpp v13, v13, v13 quad_perm:[1,0,3,2] row_mask:0xf bank_mask:0xf bound_ctrl:1
	v_add_f32_dpp v14, v14, v14 quad_perm:[1,0,3,2] row_mask:0xf bank_mask:0xf bound_ctrl:1
	v_add_f32_dpp v15, v15, v15 quad_perm:[1,0,3,2] row_mask:0xf bank_mask:0xf bound_ctrl:1
	v_add_f32_dpp v16, v16, v16 quad_perm:[1,0,3,2] row_mask:0xf bank_mask:0xf bound_ctrl:1
	v_add_f32_dpp v17, v17, v17 quad_perm:[1,0,3,2] row_mask:0xf bank_mask:0xf bound_ctrl:1
	v_add_f32_dpp v18, v18, v18 quad_perm:[1,0,3,2] row_mask:0xf bank_mask:0xf bound_ctrl:1
	v_add_f32_dpp v19, v19, v19 quad_perm:[1,0,3,2] row_mask:0xf bank_mask:0xf bound_ctrl:1
	v_add_f32_dpp v20, v20, v20 quad_perm:[1,0,3,2] row_mask:0xf bank_mask:0xf bound_ctrl:1
	v_add_f32_dpp v21, v21, v21 quad_perm:[1,0,3,2] row_mask:0xf bank_mask:0xf bound_ctrl:1
	v_add_f32_dpp v22, v22, v22 quad_perm:[1,0,3,2] row_mask:0xf bank_mask:0xf bound_ctrl:1
	v_add_f32_dpp v23, v23, v23 quad_perm:[1,0,3,2] row_mask:0xf bank_mask:0xf bound_ctrl:1
	v_add_f32_dpp v24, v24, v24 quad_perm:[1,0,3,2] row_mask:0xf bank_mask:0xf bound_ctrl:1
	v_add_f32_dpp v25, v25, v25 quad_perm:[1,0,3,2] row_mask:0xf bank_mask:0xf bound_ctrl:1
	v_add_f32_dpp v26, v26, v26 quad_perm:[1,0,3,2] row_mask:0xf bank_mask:0xf bound_ctrl:1
	v_add_f32_dpp v27, v27, v27 quad_perm:[1,0,3,2] row_mask:0xf bank_mask:0xf bound_ctrl:1
	v_add_f32_dpp v28, v28, v28 quad_perm:[1,0,3,2] row_mask:0xf bank_mask:0xf bound_ctrl:1
	v_add_f32_dpp v29, v29, v29 quad_perm:[1,0,3,2] row_mask:0xf bank_mask:0xf bound_ctrl:1
	v_add_f32_dpp v30, v30, v30 quad_perm:[1,0,3,2] row_mask:0xf bank_mask:0xf bound_ctrl:1
	v_add_f32_dpp v31, v31, v31 quad_perm:[1,0,3,2] row_mask:0xf bank_mask:0xf bound_ctrl:1
	v_add_f32_dpp v32, v32, v32 quad_perm:[1,0,3,2] row_mask:0xf bank_mask:0xf bound_ctrl:1
	v_add_f32_dpp v33, v33, v33 quad_perm:[1,0,3,2] row_mask:0xf bank_mask:0xf bound_ctrl:1
	v_add_f32_dpp v0, v0, v0 quad_perm:[1,0,3,2] row_mask:0xf bank_mask:0xf bound_ctrl:1
	v_add_f32_dpp v1, v1, v1 quad_perm:[1,0,3,2] row_mask:0xf bank_mask:0xf bound_ctrl:1
	v_add_f32_dpp v2, v2, v2 quad_perm:[1,0,3,2] row_mask:0xf bank_mask:0xf bound_ctrl:1
	v_add_f32_dpp v3, v3, v3 quad_perm:[1,0,3,2] row_mask:0xf bank_mask:0xf bound_ctrl:1
	v_add_f32_dpp v4, v4, v4 quad_perm:[1,0,3,2] row_mask:0xf bank_mask:0xf bound_ctrl:1
	v_add_f32_dpp v5, v5, v5 quad_perm:[1,0,3,2] row_mask:0xf bank_mask:0xf bound_ctrl:1
	v_add_f32_dpp v6, v6, v6 quad_perm:[1,0,3,2] row_mask:0xf bank_mask:0xf bound_ctrl:1
	v_add_f32_dpp v7, v7, v7 quad_perm:[1,0,3,2] row_mask:0xf bank_mask:0xf bound_ctrl:1
	v_add_f32_dpp v10, v10, v10 quad_perm:[2,3,0,1] row_mask:0xf bank_mask:0xf bound_ctrl:1
	v_add_f32_dpp v11, v11, v11 quad_perm:[2,3,0,1] row_mask:0xf bank_mask:0xf bound_ctrl:1
	v_add_f32_dpp v12, v12, v12 quad_perm:[2,3,0,1] row_mask:0xf bank_mask:0xf bound_ctrl:1
	v_add_f32_dpp v13, v13, v13 quad_perm:[2,3,0,1] row_mask:0xf bank_mask:0xf bound_ctrl:1
	v_add_f32_dpp v14, v14, v14 quad_perm:[2,3,0,1] row_mask:0xf bank_mask:0xf bound_ctrl:1
	v_add_f32_dpp v15, v15, v15 quad_perm:[2,3,0,1] row_mask:0xf bank_mask:0xf bound_ctrl:1
	v_add_f32_dpp v16, v16, v16 quad_perm:[2,3,0,1] row_mask:0xf bank_mask:0xf bound_ctrl:1
	v_add_f32_dpp v17, v17, v17 quad_perm:[2,3,0,1] row_mask:0xf bank_mask:0xf bound_ctrl:1
	v_add_f32_dpp v18, v18, v18 quad_perm:[2,3,0,1] row_mask:0xf bank_mask:0xf bound_ctrl:1
	v_add_f32_dpp v19, v19, v19 quad_perm:[2,3,0,1] row_mask:0xf bank_mask:0xf bound_ctrl:1
	v_add_f32_dpp v20, v20, v20 quad_perm:[2,3,0,1] row_mask:0xf bank_mask:0xf bound_ctrl:1
	v_add_f32_dpp v21, v21, v21 quad_perm:[2,3,0,1] row_mask:0xf bank_mask:0xf bound_ctrl:1
	v_add_f32_dpp v22, v22, v22 quad_perm:[2,3,0,1] row_mask:0xf bank_mask:0xf bound_ctrl:1
	v_add_f32_dpp v23, v23, v23 quad_perm:[2,3,0,1] row_mask:0xf bank_mask:0xf bound_ctrl:1
	v_add_f32_dpp v24, v24, v24 quad_perm:[2,3,0,1] row_mask:0xf bank_mask:0xf bound_ctrl:1
	v_add_f32_dpp v25, v25, v25 quad_perm:[2,3,0,1] row_mask:0xf bank_mask:0xf bound_ctrl:1
	v_add_f32_dpp v26, v26, v26 quad_perm:[2,3,0,1] row_mask:0xf bank_mask:0xf bound_ctrl:1
	v_add_f32_dpp v27, v27, v27 quad_perm:[2,3,0,1] row_mask:0xf bank_mask:0xf bound_ctrl:1
	v_add_f32_dpp v28, v28, v28 quad_perm:[2,3,0,1] row_mask:0xf bank_mask:0xf bound_ctrl:1
	v_add_f32_dpp v29, v29, v29 quad_perm:[2,3,0,1] row_mask:0xf bank_mask:0xf bound_ctrl:1
	v_add_f32_dpp v30, v30, v30 quad_perm:[2,3,0,1] row_mask:0xf bank_mask:0xf bound_ctrl:1
	v_add_f32_dpp v31, v31, v31 quad_perm:[2,3,0,1] row_mask:0xf bank_mask:0xf bound_ctrl:1
	v_add_f32_dpp v32, v32, v32 quad_perm:[2,3,0,1] row_mask:0xf bank_mask:0xf bound_ctrl:1
	v_add_f32_dpp v33, v33, v33 quad_perm:[2,3,0,1] row_mask:0xf bank_mask:0xf bound_ctrl:1
	v_add_f32_dpp v0, v0, v0 quad_perm:[2,3,0,1] row_mask:0xf bank_mask:0xf bound_ctrl:1
	v_add_f32_dpp v1, v1, v1 quad_perm:[2,3,0,1] row_mask:0xf bank_mask:0xf bound_ctrl:1
	v_add_f32_dpp v2, v2, v2 quad_perm:[2,3,0,1] row_mask:0xf bank_mask:0xf bound_ctrl:1
	v_add_f32_dpp v3, v3, v3 quad_perm:[2,3,0,1] row_mask:0xf bank_mask:0xf bound_ctrl:1
	v_add_f32_dpp v4, v4, v4 quad_perm:[2,3,0,1] row_mask:0xf bank_mask:0xf bound_ctrl:1
	v_add_f32_dpp v5, v5, v5 quad_perm:[2,3,0,1] row_mask:0xf bank_mask:0xf bound_ctrl:1
	v_add_f32_dpp v6, v6, v6 quad_perm:[2,3,0,1] row_mask:0xf bank_mask:0xf bound_ctrl:1
	v_add_f32_dpp v7, v7, v7 quad_perm:[2,3,0,1] row_mask:0xf bank_mask:0xf bound_ctrl:1
	v_add_f32_dpp v10, v10, v10 row_half_mirror row_mask:0xf bank_mask:0xf bound_ctrl:1
	v_add_f32_dpp v11, v11, v11 row_half_mirror row_mask:0xf bank_mask:0xf bound_ctrl:1
	v_add_f32_dpp v12, v12, v12 row_half_mirror row_mask:0xf bank_mask:0xf bound_ctrl:1
	v_add_f32_dpp v13, v13, v13 row_half_mirror row_mask:0xf bank_mask:0xf bound_ctrl:1
	v_add_f32_dpp v14, v14, v14 row_half_mirror row_mask:0xf bank_mask:0xf bound_ctrl:1
	v_add_f32_dpp v15, v15, v15 row_half_mirror row_mask:0xf bank_mask:0xf bound_ctrl:1
	v_add_f32_dpp v16, v16, v16 row_half_mirror row_mask:0xf bank_mask:0xf bound_ctrl:1
	v_add_f32_dpp v17, v17, v17 row_half_mirror row_mask:0xf bank_mask:0xf bound_ctrl:1
	v_add_f32_dpp v18, v18, v18 row_half_mirror row_mask:0xf bank_mask:0xf bound_ctrl:1
	v_add_f32_dpp v19, v19, v19 row_half_mirror row_mask:0xf bank_mask:0xf bound_ctrl:1
	v_add_f32_dpp v20, v20, v20 row_half_mirror row_mask:0xf bank_mask:0xf bound_ctrl:1
	v_add_f32_dpp v21, v21, v21 row_half_mirror row_mask:0xf bank_mask:0xf bound_ctrl:1
	v_add_f32_dpp v22, v22, v22 row_half_mirror row_mask:0xf bank_mask:0xf bound_ctrl:1
	v_add_f32_dpp v23, v23, v23 row_half_mirror row_mask:0xf bank_mask:0xf bound_ctrl:1
	v_add_f32_dpp v24, v24, v24 row_half_mirror row_mask:0xf bank_mask:0xf bound_ctrl:1
	v_add_f32_dpp v25, v25, v25 row_half_mirror row_mask:0xf bank_mask:0xf bound_ctrl:1
	v_add_f32_dpp v26, v26, v26 row_half_mirror row_mask:0xf bank_mask:0xf bound_ctrl:1
	v_add_f32_dpp v27, v27, v27 row_half_mirror row_mask:0xf bank_mask:0xf bound_ctrl:1
	v_add_f32_dpp v28, v28, v28 row_half_mirror row_mask:0xf bank_mask:0xf bound_ctrl:1
	v_add_f32_dpp v29, v29, v29 row_half_mirror row_mask:0xf bank_mask:0xf bound_ctrl:1
	v_add_f32_dpp v30, v30, v30 row_half_mirror row_mask:0xf bank_mask:0xf bound_ctrl:1
	v_add_f32_dpp v31, v31, v31 row_half_mirror row_mask:0xf bank_mask:0xf bound_ctrl:1
	v_add_f32_dpp v32, v32, v32 row_half_mirror row_mask:0xf bank_mask:0xf bound_ctrl:1
	v_add_f32_dpp v33, v33, v33 row_half_mirror row_mask:0xf bank_mask:0xf bound_ctrl:1
	v_add_f32_dpp v0, v0, v0 row_half_mirror row_mask:0xf bank_mask:0xf bound_ctrl:1
	v_add_f32_dpp v1, v1, v1 row_half_mirror row_mask:0xf bank_mask:0xf bound_ctrl:1
	v_add_f32_dpp v2, v2, v2 row_half_mirror row_mask:0xf bank_mask:0xf bound_ctrl:1
	v_add_f32_dpp v3, v3, v3 row_half_mirror row_mask:0xf bank_mask:0xf bound_ctrl:1
	v_add_f32_dpp v4, v4, v4 row_half_mirror row_mask:0xf bank_mask:0xf bound_ctrl:1
	v_add_f32_dpp v5, v5, v5 row_half_mirror row_mask:0xf bank_mask:0xf bound_ctrl:1
	v_add_f32_dpp v6, v6, v6 row_half_mirror row_mask:0xf bank_mask:0xf bound_ctrl:1
	v_add_f32_dpp v7, v7, v7 row_half_mirror row_mask:0xf bank_mask:0xf bound_ctrl:1
	v_add_f32_dpp v10, v10, v10 row_mirror row_mask:0xf bank_mask:0xf bound_ctrl:1
	v_add_f32_dpp v11, v11, v11 row_mirror row_mask:0xf bank_mask:0xf bound_ctrl:1
	v_add_f32_dpp v12, v12, v12 row_mirror row_mask:0xf bank_mask:0xf bound_ctrl:1
	v_add_f32_dpp v13, v13, v13 row_mirror row_mask:0xf bank_mask:0xf bound_ctrl:1
	v_add_f32_dpp v14, v14, v14 row_mirror row_mask:0xf bank_mask:0xf bound_ctrl:1
	v_add_f32_dpp v15, v15, v15 row_mirror row_mask:0xf bank_mask:0xf bound_ctrl:1
	v_add_f32_dpp v16, v16, v16 row_mirror row_mask:0xf bank_mask:0xf bound_ctrl:1
	v_add_f32_dpp v17, v17, v17 row_mirror row_mask:0xf bank_mask:0xf bound_ctrl:1
	v_add_f32_dpp v18, v18, v18 row_mirror row_mask:0xf bank_mask:0xf bound_ctrl:1
	v_add_f32_dpp v19, v19, v19 row_mirror row_mask:0xf bank_mask:0xf bound_ctrl:1
	v_add_f32_dpp v20, v20, v20 row_mirror row_mask:0xf bank_mask:0xf bound_ctrl:1
	v_add_f32_dpp v21, v21, v21 row_mirror row_mask:0xf bank_mask:0xf bound_ctrl:1
	v_add_f32_dpp v22, v22, v22 row_mirror row_mask:0xf bank_mask:0xf bound_ctrl:1
	v_add_f32_dpp v23, v23, v23 row_mirror row_mask:0xf bank_mask:0xf bound_ctrl:1
	v_add_f32_dpp v24, v24, v24 row_mirror row_mask:0xf bank_mask:0xf bound_ctrl:1
	v_add_f32_dpp v25, v25, v25 row_mirror row_mask:0xf bank_mask:0xf bound_ctrl:1
	v_add_f32_dpp v26, v26, v26 row_mirror row_mask:0xf bank_mask:0xf bound_ctrl:1
	v_add_f32_dpp v27, v27, v27 row_mirror row_mask:0xf bank_mask:0xf bound_ctrl:1
	v_add_f32_dpp v28, v28, v28 row_mirror row_mask:0xf bank_mask:0xf bound_ctrl:1
	v_add_f32_dpp v29, v29, v29 row_mirror row_mask:0xf bank_mask:0xf bound_ctrl:1
	v_add_f32_dpp v30, v30, v30 row_mirror row_mask:0xf bank_mask:0xf bound_ctrl:1
	v_add_f32_dpp v31, v31, v31 row_mirror row_mask:0xf bank_mask:0xf bound_ctrl:1
	v_add_f32_dpp v32, v32, v32 row_mirror row_mask:0xf bank_mask:0xf bound_ctrl:1
	v_add_f32_dpp v33, v33, v33 row_mirror row_mask:0xf bank_mask:0xf bound_ctrl:1
	v_add_f32_dpp v0, v0, v0 row_mirror row_mask:0xf bank_mask:0xf bound_ctrl:1
	v_add_f32_dpp v1, v1, v1 row_mirror row_mask:0xf bank_mask:0xf bound_ctrl:1
	v_add_f32_dpp v2, v2, v2 row_mirror row_mask:0xf bank_mask:0xf bound_ctrl:1
	v_add_f32_dpp v3, v3, v3 row_mirror row_mask:0xf bank_mask:0xf bound_ctrl:1
	v_add_f32_dpp v4, v4, v4 row_mirror row_mask:0xf bank_mask:0xf bound_ctrl:1
	v_add_f32_dpp v5, v5, v5 row_mirror row_mask:0xf bank_mask:0xf bound_ctrl:1
	v_add_f32_dpp v6, v6, v6 row_mirror row_mask:0xf bank_mask:0xf bound_ctrl:1
	v_add_f32_dpp v7, v7, v7 row_mirror row_mask:0xf bank_mask:0xf bound_ctrl:1
	v_add_f32_dpp v10, v10, v10 row_bcast:15 row_mask:0xa bank_mask:0xf
	v_add_f32_dpp v11, v11, v11 row_bcast:15 row_mask:0xa bank_mask:0xf
	v_add_f32_dpp v12, v12, v12 row_bcast:15 row_mask:0xa bank_mask:0xf
	v_add_f32_dpp v13, v13, v13 row_bcast:15 row_mask:0xa bank_mask:0xf
	v_add_f32_dpp v14, v14, v14 row_bcast:15 row_mask:0xa bank_mask:0xf
	v_add_f32_dpp v15, v15, v15 row_bcast:15 row_mask:0xa bank_mask:0xf
	v_add_f32_dpp v16, v16, v16 row_bcast:15 row_mask:0xa bank_mask:0xf
	v_add_f32_dpp v17, v17, v17 row_bcast:15 row_mask:0xa bank_mask:0xf
	v_add_f32_dpp v18, v18, v18 row_bcast:15 row_mask:0xa bank_mask:0xf
	v_add_f32_dpp v19, v19, v19 row_bcast:15 row_mask:0xa bank_mask:0xf
	v_add_f32_dpp v20, v20, v20 row_bcast:15 row_mask:0xa bank_mask:0xf
	v_add_f32_dpp v21, v21, v21 row_bcast:15 row_mask:0xa bank_mask:0xf
	v_add_f32_dpp v22, v22, v22 row_bcast:15 row_mask:0xa bank_mask:0xf
	v_add_f32_dpp v23, v23, v23 row_bcast:15 row_mask:0xa bank_mask:0xf
	v_add_f32_dpp v24, v24, v24 row_bcast:15 row_mask:0xa bank_mask:0xf
	v_add_f32_dpp v25, v25, v25 row_bcast:15 row_mask:0xa bank_mask:0xf
	v_add_f32_dpp v26, v26, v26 row_bcast:15 row_mask:0xa bank_mask:0xf
	v_add_f32_dpp v27, v27, v27 row_bcast:15 row_mask:0xa bank_mask:0xf
	v_add_f32_dpp v28, v28, v28 row_bcast:15 row_mask:0xa bank_mask:0xf
	v_add_f32_dpp v29, v29, v29 row_bcast:15 row_mask:0xa bank_mask:0xf
	v_add_f32_dpp v30, v30, v30 row_bcast:15 row_mask:0xa bank_mask:0xf
	v_add_f32_dpp v31, v31, v31 row_bcast:15 row_mask:0xa bank_mask:0xf
	v_add_f32_dpp v32, v32, v32 row_bcast:15 row_mask:0xa bank_mask:0xf
	v_add_f32_dpp v33, v33, v33 row_bcast:15 row_mask:0xa bank_mask:0xf
	v_add_f32_dpp v0, v0, v0 row_bcast:15 row_mask:0xa bank_mask:0xf
	v_add_f32_dpp v1, v1, v1 row_bcast:15 row_mask:0xa bank_mask:0xf
	v_add_f32_dpp v2, v2, v2 row_bcast:15 row_mask:0xa bank_mask:0xf
	v_add_f32_dpp v3, v3, v3 row_bcast:15 row_mask:0xa bank_mask:0xf
	v_add_f32_dpp v4, v4, v4 row_bcast:15 row_mask:0xa bank_mask:0xf
	v_add_f32_dpp v5, v5, v5 row_bcast:15 row_mask:0xa bank_mask:0xf
	v_add_f32_dpp v6, v6, v6 row_bcast:15 row_mask:0xa bank_mask:0xf
	v_add_f32_dpp v7, v7, v7 row_bcast:15 row_mask:0xa bank_mask:0xf
	v_add_f32_dpp v10, v10, v10 row_bcast:31 row_mask:0xc bank_mask:0xf
	v_add_f32_dpp v11, v11, v11 row_bcast:31 row_mask:0xc bank_mask:0xf
	v_add_f32_dpp v12, v12, v12 row_bcast:31 row_mask:0xc bank_mask:0xf
	v_add_f32_dpp v13, v13, v13 row_bcast:31 row_mask:0xc bank_mask:0xf
	v_add_f32_dpp v14, v14, v14 row_bcast:31 row_mask:0xc bank_mask:0xf
	v_add_f32_dpp v15, v15, v15 row_bcast:31 row_mask:0xc bank_mask:0xf
	v_add_f32_dpp v16, v16, v16 row_bcast:31 row_mask:0xc bank_mask:0xf
	v_add_f32_dpp v17, v17, v17 row_bcast:31 row_mask:0xc bank_mask:0xf
	v_add_f32_dpp v18, v18, v18 row_bcast:31 row_mask:0xc bank_mask:0xf
	v_add_f32_dpp v19, v19, v19 row_bcast:31 row_mask:0xc bank_mask:0xf
	v_add_f32_dpp v20, v20, v20 row_bcast:31 row_mask:0xc bank_mask:0xf
	v_add_f32_dpp v21, v21, v21 row_bcast:31 row_mask:0xc bank_mask:0xf
	v_add_f32_dpp v22, v22, v22 row_bcast:31 row_mask:0xc bank_mask:0xf
	v_add_f32_dpp v23, v23, v23 row_bcast:31 row_mask:0xc bank_mask:0xf
	v_add_f32_dpp v24, v24, v24 row_bcast:31 row_mask:0xc bank_mask:0xf
	v_add_f32_dpp v25, v25, v25 row_bcast:31 row_mask:0xc bank_mask:0xf
	v_add_f32_dpp v26, v26, v26 row_bcast:31 row_mask:0xc bank_mask:0xf
	v_add_f32_dpp v27, v27, v27 row_bcast:31 row_mask:0xc bank_mask:0xf
	v_add_f32_dpp v28, v28, v28 row_bcast:31 row_mask:0xc bank_mask:0xf
	v_add_f32_dpp v29, v29, v29 row_bcast:31 row_mask:0xc bank_mask:0xf
	v_add_f32_dpp v30, v30, v30 row_bcast:31 row_mask:0xc bank_mask:0xf
	v_add_f32_dpp v31, v31, v31 row_bcast:31 row_mask:0xc bank_mask:0xf
	v_add_f32_dpp v32, v32, v32 row_bcast:31 row_mask:0xc bank_mask:0xf
	v_add_f32_dpp v33, v33, v33 row_bcast:31 row_mask:0xc bank_mask:0xf
	v_add_f32_dpp v0, v0, v0 row_bcast:31 row_mask:0xc bank_mask:0xf
	v_add_f32_dpp v1, v1, v1 row_bcast:31 row_mask:0xc bank_mask:0xf
	v_add_f32_dpp v2, v2, v2 row_bcast:31 row_mask:0xc bank_mask:0xf
	v_add_f32_dpp v3, v3, v3 row_bcast:31 row_mask:0xc bank_mask:0xf
	v_add_f32_dpp v4, v4, v4 row_bcast:31 row_mask:0xc bank_mask:0xf
	v_add_f32_dpp v5, v5, v5 row_bcast:31 row_mask:0xc bank_mask:0xf
	v_add_f32_dpp v6, v6, v6 row_bcast:31 row_mask:0xc bank_mask:0xf
	v_add_f32_dpp v7, v7, v7 row_bcast:31 row_mask:0xc bank_mask:0xf
	s_add_i32 s28, s36, 0x1f000
	v_mov_b32_e32 v64, s28
	s_mov_b32 exec_lo, 0
	s_brev_b32 exec_hi, 1
	ds_write_b64 v64, v[10:11]
	ds_write_b64 v64, v[12:13] offset:8
	ds_write_b64 v64, v[14:15] offset:16
	ds_write_b64 v64, v[16:17] offset:24
	ds_write_b64 v64, v[18:19] offset:32
	ds_write_b64 v64, v[20:21] offset:40
	ds_write_b64 v64, v[22:23] offset:48
	ds_write_b64 v64, v[24:25] offset:56
	ds_write_b64 v64, v[26:27] offset:64
	ds_write_b64 v64, v[28:29] offset:72
	ds_write_b64 v64, v[30:31] offset:80
	ds_write_b64 v64, v[32:33] offset:88
	ds_write_b64 v64, v[0:1] offset:96
	ds_write_b64 v64, v[2:3] offset:104
	ds_write_b64 v64, v[4:5] offset:112
	ds_write_b64 v64, v[6:7] offset:120
	s_mov_b64 exec, -1
	s_waitcnt lgkmcnt(0)
	s_barrier
	s_and_saveexec_b64 s[28:29], s[6:7]
	s_cbranch_execz .LBB0_597
	ds_read2_b64 v[0:3], v199 offset1:16
	s_mov_b32 s30, 0x3b000000
	s_waitcnt lgkmcnt(0)
	v_add_f32_e32 v0, 0, v0
	v_add_f32_e32 v1, 0, v1
	v_add_f32_e32 v4, v0, v2
	v_add_f32_e32 v5, v1, v3
	ds_read2_b64 v[0:3], v199 offset0:32 offset1:48
	s_waitcnt lgkmcnt(0)
	v_add_f32_e32 v0, v4, v0
	v_add_f32_e32 v0, v0, v2
	v_add_f32_e32 v1, v5, v1
	v_mul_f32_e32 v0, 0x3b000000, v0
	v_add_f32_e32 v1, v1, v3
	v_mul_f32_e32 v2, v0, v0
	v_fma_f32 v1, v1, s30, -v2
	v_max_f32_e32 v1, 0, v1
	v_add_f32_e32 v1, 0x358637bd, v1
	v_rsq_f32_e32 v1, v1
	ds_write_b64 v169, v[0:1]
	s_branch .LBB0_597
